# speedup vs baseline: 1.0111x; 1.0111x over previous
.LBB1_107:
	v_and_b32_e32 v98, 48, v179
	v_readlane_b32 s18, v240, 24
	v_add_u32_e32 v108, 0, v98
	v_add_u32_e32 v108, 0x18400, v108
	v_add_u32_e32 v162, s18, v98
	s_waitcnt lgkmcnt(0)
	s_barrier
	ds_read_b128 v[138:141], v108
	ds_read_b128 v[142:145], v108 offset:64
	ds_read_b128 v[146:149], v108 offset:128
	ds_read_b128 v[150:153], v108 offset:192
	ds_read_b128 v[154:157], v162
	ds_read_b128 v[158:161], v162 offset:64
	s_waitcnt vmcnt(7) lgkmcnt(5)
	v_mfma_f32_16x16x32_f16 v[130:133], v[130:133], v[138:141], 0
	s_waitcnt vmcnt(3)
	v_mfma_f32_16x16x32_f16 v[134:137], v[134:137], v[138:141], 0
	s_waitcnt lgkmcnt(4)
	v_mfma_f32_16x16x32_f16 v[114:117], v[114:117], v[142:145], v[130:133]
	s_waitcnt vmcnt(2)
	v_mfma_f32_16x16x32_f16 v[122:125], v[122:125], v[142:145], v[134:137]
	s_waitcnt lgkmcnt(3)
	v_mfma_f32_16x16x32_f16 v[114:117], v[118:121], v[146:149], v[114:117]
	s_waitcnt vmcnt(1)
	v_mfma_f32_16x16x32_f16 v[118:121], v[126:129], v[146:149], v[122:125]
	s_waitcnt lgkmcnt(2)
	v_mfma_f32_16x16x32_f16 v[114:117], v[104:107], v[150:153], v[114:117]
	v_and_b32_e32 v104, 15, v179
	v_cmp_eq_u32_e32 vcc, 0, v104
	s_waitcnt vmcnt(0)
	v_mfma_f32_16x16x32_f16 v[104:107], v[110:113], v[150:153], v[118:121]
	s_and_saveexec_b64 s[0:1], vcc
	s_cbranch_execz .LBB1_115
	s_cmp_lg_u32 s30, 31
	v_lshrrev_b32_e32 v103, 2, v103
	s_nop 7
	s_cselect_b64 s[20:21], -1, 0
	s_and_b64 vcc, exec, s[20:21]
	s_waitcnt lgkmcnt(0)
	v_add_f32_e32 v108, v114, v154
	v_add_f32_e32 v110, v115, v155
	v_add_f32_e32 v108, v108, v108
	v_add_f32_e32 v110, v110, v110
	v_mul_f32_e32 v108, 0x3fb8aa3b, v108
	v_exp_f32_e32 v108, v108
	v_mul_f32_e32 v110, 0x3fb8aa3b, v110
	v_exp_f32_e32 v115, v110
	v_add_f32_e32 v98, 1.0, v108
	v_add_f32_e32 v108, v116, v156
	v_rcp_f32_e32 v114, v98
	v_add_f32_e32 v98, 1.0, v115
	v_add_f32_e32 v108, v108, v108
	v_add_f32_e32 v115, v117, v157
	v_mul_f32_e32 v108, 0x3fb8aa3b, v108
	v_add_f32_e32 v115, v115, v115
	v_exp_f32_e32 v108, v108
	v_mul_f32_e32 v115, 0x3fb8aa3b, v115
	v_exp_f32_e32 v117, v115
	v_rcp_f32_e32 v115, v98
	v_add_f32_e32 v98, 1.0, v108
	v_rcp_f32_e32 v116, v98
	v_add_f32_e32 v98, 1.0, v117
	v_rcp_f32_e32 v117, v98
	v_or_b32_e32 v98, s71, v103
	v_pk_fma_f32 v[114:115], v[114:115], 2.0, 1.0 op_sel_hi:[1,0,0] neg_lo:[1,0,0] neg_hi:[1,0,0]
	v_pk_fma_f32 v[116:117], v[116:117], 2.0, 1.0 op_sel_hi:[1,0,0] neg_lo:[1,0,0] neg_hi:[1,0,0]
	s_cbranch_vccnz .LBB1_110
	v_readlane_b32 s18, v240, 18
	v_mov_b32_e32 v119, v99
	v_readlane_b32 s19, v240, 19
	v_add_u32_e32 v118, s18, v98
	v_lshl_add_u64 v[118:119], v[118:119], 2, s[60:61]
	global_store_dwordx4 v[118:119], v[114:117], off

.LBB1_112:
	s_waitcnt lgkmcnt(0)
	v_add_f32_e32 v104, v104, v158
	v_add_f32_e32 v105, v105, v159
	v_add_f32_e32 v106, v106, v160
	v_add_f32_e32 v107, v107, v161
	v_add_f32_e32 v104, v104, v104
	v_add_f32_e32 v105, v105, v105
	v_add_f32_e32 v106, v106, v106
	v_add_f32_e32 v107, v107, v107
	v_mul_f32_e32 v104, 0x3fb8aa3b, v104
	v_mul_f32_e32 v105, 0x3fb8aa3b, v105
	v_mul_f32_e32 v106, 0x3fb8aa3b, v106
	v_mul_f32_e32 v107, 0x3fb8aa3b, v107
	v_exp_f32_e32 v104, v104
	v_exp_f32_e32 v105, v105
	v_exp_f32_e32 v106, v106
	v_exp_f32_e32 v107, v107
	v_add_f32_e32 v104, 1.0, v104
	v_add_f32_e32 v105, 1.0, v105
	v_add_f32_e32 v106, 1.0, v106
	v_add_f32_e32 v107, 1.0, v107
	v_rcp_f32_e32 v104, v104
	v_rcp_f32_e32 v105, v105
	v_rcp_f32_e32 v106, v106
	v_rcp_f32_e32 v107, v107
	s_andn2_b64 vcc, exec, s[98:99]
	v_pk_fma_f32 v[104:105], v[104:105], 2.0, 1.0 op_sel_hi:[1,0,0] neg_lo:[1,0,0] neg_hi:[1,0,0]
	v_pk_fma_f32 v[106:107], v[106:107], 2.0, 1.0 op_sel_hi:[1,0,0] neg_lo:[1,0,0] neg_hi:[1,0,0]
	s_cbranch_vccnz .LBB1_114
	v_readlane_b32 s20, v240, 18
	v_readlane_b32 s21, v240, 19
	s_nop 1
	v_lshl_add_u64 v[110:111], v[98:99], 0, s[20:21]
	v_lshl_add_u64 v[110:111], v[110:111], 2, s[60:61]
	global_store_dwordx4 v[110:111], v[104:107], off offset:64
